# MoE XCD grouping applied only when the grid has 256 workgroups
# speedup vs baseline: 1.0108x; 1.0006x over previous
; #define LAS __attribute__((address_space(3)))
;     __device__ __forceinline__ bool next(int i, Unit& u) const {
;         const int nm = c < nmain ? (nmain - c + G - 1) / G : 0;
;         int L; u.sub = -1;
;         if (i < nm) L = i * G + c;
;         else if (i == nm && tail > 0 && c / ways < tail) { L = nmain + c / ways; u.sub = ways == 4 ? (c & 3) : 4 + (c & 1); }
;         else return false;
;         const int rt = L >> 3; u.pm = rt; u.pn = rt_exp[rt] * 8 + (L & 7); return true; }
; __device__ __forceinline__ void ph_moe1(const Frame& F) {
;     LAS int* offs = (LAS int*)(F.lds + LDS_TAB); LAS int* cnts = offs + 128; LAS int* rt_exp = offs + 256;
;     expert_offsets(F, offs, cnts, rt_exp);
;     pg8::GroupedOrder So; So.init(rt_exp, (offs[64] >> 8) * 8, (int)gridDim.x, (int)blockIdx.x);
.LBB0_1008:
	v_writelane_b32 v248, s97, 60
	v_readlane_b32 s0, v248, 0
	v_readlane_b32 s1, v248, 1
	s_load_dword s74, s[0:1], 0xd0
	s_waitcnt lgkmcnt(0)
	s_cmpk_lg_u32 s74, 0x100
	s_cbranch_scc1 .Lmoe_noremap
	s_and_b32 s0, s97, 7
	s_lshr_b32 s1, s97, 3
	s_lshr_b32 s74, s0, 1
	s_lshl_b32 s74, s74, 3
	s_lshr_b32 s75, s1, 2
	s_add_i32 s74, s74, s75
	s_lshl_b32 s74, s74, 3
	s_and_b32 s0, s0, 1
	s_lshl_b32 s0, s0, 2
	s_and_b32 s1, s1, 3
	s_or_b32 s0, s0, s1
	s_or_b32 s97, s74, s0
